# out-GEMM EpiResid epilogue de-serialised: 8 residual loads in flight with counted vmcnt instead of load-wait-store per block (on top of ret-scan v1)
# speedup vs baseline: 1.0085x; 1.0085x over previous
; __device__ __forceinline__ unsigned cvt_pk_bf16(float lo, float hi) { unsigned r; asm volatile("v_cvt_pk_bf16_f32 %0, %1, %2" : "=v"(r) : "v"(lo), "v"(hi)); return r; }
;     __device__ __forceinline__ void operator()(const f32x4 (&acc)[2][2][4][2], const Unit& u, int wr, int wc, int fr, int fq) const {
;     ...
;         for (int ai = 0; ai < 2; ++ai)
; #pragma unroll
;             for (int m = 0; m < 4; ++m) { const size_t ro = (size_t)(row0 + ai * HALF + m * 16) * DM + col0;
; #pragma unroll
;                 for (int bj = 0; bj < 2; ++bj) {
;                     f32x4 h0, h1;
;                     if (xin) { h0 = *(const f32x4*)(xin + ro + bj * HALF); h1 = *(const f32x4*)(xin + ro + bj * HALF + 4); }
;                     else { const u32x4 hb = *(const u32x4*)(hin + ro + bj * HALF);
;                         h0 = (f32x4){__builtin_bit_cast(float, hb.x << 16), __builtin_bit_cast(float, hb.x & 0xffff0000u), __builtin_bit_cast(float, hb.y << 16), __builtin_bit_cast(float, hb.y & 0xffff0000u)};
;                         h1 = (f32x4){__builtin_bit_cast(float, hb.z << 16), __builtin_bit_cast(float, hb.z & 0xffff0000u), __builtin_bit_cast(float, hb.w << 16), __builtin_bit_cast(float, hb.w & 0xffff0000u)}; }
;                     const f32x4 o0 = h0 + gv[bj][0] * acc[ai][bj][m][0], o1 = h1 + gv[bj][1] * acc[ai][bj][m][1];
;                     u32x4 w; w.x = cvt_pk_bf16(o0[0], o0[1]); w.y = cvt_pk_bf16(o0[2], o0[3]); w.z = cvt_pk_bf16(o1[0], o1[1]); w.w = cvt_pk_bf16(o1[2], o1[3]);
;                     *(u32x4*)(hout + ro + bj * HALF) = w; } }
.Lepi_done:
	s_cbranch_vccnz .LBB0_939
	s_andn2_b64 vcc, exec, s[12:13]
	s_cbranch_vccnz .LBB0_938
	s_barrier
	s_branch .LBB0_938
.LBB0_1013:
	v_lshl_add_u64 v[222:223], v[168:169], 1, s[18:19]
	s_mov_b32 s92, 0x10000
	s_mov_b32 s93, 0
	s_mov_b32 s94, 0x50000
	s_mov_b32 s95, 0
	v_mov_b64_e32 v[224:225], v[222:223]
	global_load_dwordx4 v[180:183], v[222:223], off
	global_load_dwordx4 v[184:187], v[222:223], off offset:256
	v_lshl_add_u64 v[222:223], v[222:223], 0, s[92:93]
	global_load_dwordx4 v[188:191], v[222:223], off
	global_load_dwordx4 v[202:205], v[222:223], off offset:256
	v_lshl_add_u64 v[222:223], v[222:223], 0, s[92:93]
	global_load_dwordx4 v[206:209], v[222:223], off
	global_load_dwordx4 v[210:213], v[222:223], off offset:256
	v_lshl_add_u64 v[222:223], v[222:223], 0, s[92:93]
	global_load_dwordx4 v[214:217], v[222:223], off
	global_load_dwordx4 v[218:221], v[222:223], off offset:256
	v_lshl_add_u64 v[222:223], v[222:223], 0, s[94:95]
	s_waitcnt vmcnt(7)
	v_lshlrev_b32_e32 v146, 16, v180
	v_and_b32_e32 v147, 0xffff0000, v180
	v_lshlrev_b32_e32 v148, 16, v181
	v_and_b32_e32 v149, 0xffff0000, v181
	v_lshlrev_b32_e32 v150, 16, v182
	v_and_b32_e32 v151, 0xffff0000, v182
	v_lshlrev_b32_e32 v152, 16, v183
	v_and_b32_e32 v153, 0xffff0000, v183
	v_pk_fma_f32 v[142:143], v[142:143], v[82:83], v[146:147]
	v_pk_fma_f32 v[146:147], v[140:141], v[88:89], v[152:153]
	v_pk_fma_f32 v[140:141], v[138:139], v[86:87], v[150:151]
	v_pk_fma_f32 v[144:145], v[144:145], v[84:85], v[148:149]
	v_cvt_pk_bf16_f32 v138, v142, v143
	s_nop 0
	v_cvt_pk_bf16_f32 v139, v144, v145
	v_cvt_pk_bf16_f32 v140, v140, v141
	v_cvt_pk_bf16_f32 v141, v146, v147
	global_store_dwordx4 v[224:225], v[138:141], off
	s_nop 1
	global_load_dwordx4 v[180:183], v[222:223], off
	s_waitcnt vmcnt(8)
	v_lshlrev_b32_e32 v138, 16, v184
	v_and_b32_e32 v139, 0xffff0000, v184
	v_lshlrev_b32_e32 v140, 16, v185
	v_and_b32_e32 v141, 0xffff0000, v185
	v_lshlrev_b32_e32 v142, 16, v186
	v_and_b32_e32 v143, 0xffff0000, v186
	v_lshlrev_b32_e32 v144, 16, v187
	v_and_b32_e32 v145, 0xffff0000, v187
	v_pk_fma_f32 v[134:135], v[134:135], v[74:75], v[138:139]
	v_pk_fma_f32 v[138:139], v[132:133], v[80:81], v[144:145]
	v_pk_fma_f32 v[132:133], v[130:131], v[78:79], v[142:143]
	v_cvt_pk_bf16_f32 v130, v134, v135
	v_pk_fma_f32 v[136:137], v[136:137], v[76:77], v[140:141]
	v_cvt_pk_bf16_f32 v131, v136, v137
	v_cvt_pk_bf16_f32 v132, v132, v133
	v_cvt_pk_bf16_f32 v133, v138, v139
	global_store_dwordx4 v[224:225], v[130:133], off offset:256
	s_nop 1
	v_lshl_add_u64 v[224:225], v[224:225], 0, s[92:93]
	global_load_dwordx4 v[184:187], v[222:223], off offset:256
	v_lshl_add_u64 v[222:223], v[222:223], 0, s[92:93]
	s_waitcnt vmcnt(9)
	v_lshlrev_b32_e32 v130, 16, v188
	v_and_b32_e32 v131, 0xffff0000, v188
	v_lshlrev_b32_e32 v132, 16, v189
	v_and_b32_e32 v133, 0xffff0000, v189
	v_lshlrev_b32_e32 v134, 16, v190
	v_and_b32_e32 v135, 0xffff0000, v190
	v_lshlrev_b32_e32 v136, 16, v191
	v_and_b32_e32 v137, 0xffff0000, v191
	v_pk_fma_f32 v[126:127], v[126:127], v[82:83], v[130:131]
	v_pk_fma_f32 v[130:131], v[124:125], v[88:89], v[136:137]
	v_pk_fma_f32 v[124:125], v[122:123], v[86:87], v[134:135]
	v_pk_fma_f32 v[128:129], v[128:129], v[84:85], v[132:133]
	v_cvt_pk_bf16_f32 v122, v126, v127
	s_nop 0
	v_cvt_pk_bf16_f32 v123, v128, v129
	v_cvt_pk_bf16_f32 v124, v124, v125
	v_cvt_pk_bf16_f32 v125, v130, v131
	global_store_dwordx4 v[224:225], v[122:125], off
	s_nop 1
	global_load_dwordx4 v[188:191], v[222:223], off
	s_waitcnt vmcnt(10)
	v_lshlrev_b32_e32 v122, 16, v202
	v_and_b32_e32 v123, 0xffff0000, v202
	v_lshlrev_b32_e32 v124, 16, v203
	v_and_b32_e32 v125, 0xffff0000, v203
	v_lshlrev_b32_e32 v126, 16, v204
	v_and_b32_e32 v127, 0xffff0000, v204
	v_lshlrev_b32_e32 v128, 16, v205
	v_and_b32_e32 v129, 0xffff0000, v205
	v_pk_fma_f32 v[118:119], v[118:119], v[74:75], v[122:123]
	v_pk_fma_f32 v[122:123], v[116:117], v[80:81], v[128:129]
	v_pk_fma_f32 v[116:117], v[114:115], v[78:79], v[126:127]
	v_cvt_pk_bf16_f32 v114, v118, v119
	v_pk_fma_f32 v[120:121], v[120:121], v[76:77], v[124:125]
	v_cvt_pk_bf16_f32 v115, v120, v121
	v_cvt_pk_bf16_f32 v116, v116, v117
	v_cvt_pk_bf16_f32 v117, v122, v123
	global_store_dwordx4 v[224:225], v[114:117], off offset:256
	s_nop 1
	v_lshl_add_u64 v[224:225], v[224:225], 0, s[92:93]
	global_load_dwordx4 v[202:205], v[222:223], off offset:256
	v_lshl_add_u64 v[222:223], v[222:223], 0, s[92:93]
	s_waitcnt vmcnt(11)
	v_lshlrev_b32_e32 v114, 16, v206
	v_and_b32_e32 v115, 0xffff0000, v206
	v_lshlrev_b32_e32 v116, 16, v207
	v_and_b32_e32 v117, 0xffff0000, v207
	v_lshlrev_b32_e32 v118, 16, v208
	v_and_b32_e32 v119, 0xffff0000, v208
	v_lshlrev_b32_e32 v120, 16, v209
	v_and_b32_e32 v121, 0xffff0000, v209
	v_pk_fma_f32 v[110:111], v[110:111], v[82:83], v[114:115]
	v_pk_fma_f32 v[114:115], v[108:109], v[88:89], v[120:121]
	v_pk_fma_f32 v[108:109], v[106:107], v[86:87], v[118:119]
	v_pk_fma_f32 v[112:113], v[112:113], v[84:85], v[116:117]
	v_cvt_pk_bf16_f32 v106, v110, v111
	s_nop 0
	v_cvt_pk_bf16_f32 v107, v112, v113
	v_cvt_pk_bf16_f32 v108, v108, v109
	v_cvt_pk_bf16_f32 v109, v114, v115
	global_store_dwordx4 v[224:225], v[106:109], off
	s_nop 1
	global_load_dwordx4 v[206:209], v[222:223], off
	s_waitcnt vmcnt(12)
; __device__ __forceinline__ unsigned cvt_pk_bf16(float lo, float hi) { unsigned r; asm volatile("v_cvt_pk_bf16_f32 %0, %1, %2" : "=v"(r) : "v"(lo), "v"(hi)); return r; }
;     __device__ __forceinline__ void operator()(const f32x4 (&acc)[2][2][4][2], const Unit& u, int wr, int wc, int fr, int fq) const {
;     ...
;         for (int ai = 0; ai < 2; ++ai)
; #pragma unroll
;             for (int m = 0; m < 4; ++m) { const size_t ro = (size_t)(row0 + ai * HALF + m * 16) * DM + col0;
; #pragma unroll
;                 for (int bj = 0; bj < 2; ++bj) {
;                     f32x4 h0, h1;
;                     if (xin) { h0 = *(const f32x4*)(xin + ro + bj * HALF); h1 = *(const f32x4*)(xin + ro + bj * HALF + 4); }
;                     else { const u32x4 hb = *(const u32x4*)(hin + ro + bj * HALF);
;                         h0 = (f32x4){__builtin_bit_cast(float, hb.x << 16), __builtin_bit_cast(float, hb.x & 0xffff0000u), __builtin_bit_cast(float, hb.y << 16), __builtin_bit_cast(float, hb.y & 0xffff0000u)};
;                         h1 = (f32x4){__builtin_bit_cast(float, hb.z << 16), __builtin_bit_cast(float, hb.z & 0xffff0000u), __builtin_bit_cast(float, hb.w << 16), __builtin_bit_cast(float, hb.w & 0xffff0000u)}; }
;                     const f32x4 o0 = h0 + gv[bj][0] * acc[ai][bj][m][0], o1 = h1 + gv[bj][1] * acc[ai][bj][m][1];
;                     u32x4 w; w.x = cvt_pk_bf16(o0[0], o0[1]); w.y = cvt_pk_bf16(o0[2], o0[3]); w.z = cvt_pk_bf16(o1[0], o1[1]); w.w = cvt_pk_bf16(o1[2], o1[3]);
;                     *(u32x4*)(hout + ro + bj * HALF) = w; } }
	v_lshlrev_b32_e32 v106, 16, v210
	v_and_b32_e32 v107, 0xffff0000, v210
	v_lshlrev_b32_e32 v108, 16, v211
	v_and_b32_e32 v109, 0xffff0000, v211
	v_lshlrev_b32_e32 v110, 16, v212
	v_and_b32_e32 v111, 0xffff0000, v212
	v_lshlrev_b32_e32 v112, 16, v213
	v_and_b32_e32 v113, 0xffff0000, v213
	v_pk_fma_f32 v[102:103], v[102:103], v[74:75], v[106:107]
	v_pk_fma_f32 v[106:107], v[100:101], v[80:81], v[112:113]
	v_pk_fma_f32 v[100:101], v[98:99], v[78:79], v[110:111]
	v_cvt_pk_bf16_f32 v98, v102, v103
	v_pk_fma_f32 v[104:105], v[104:105], v[76:77], v[108:109]
	v_cvt_pk_bf16_f32 v99, v104, v105
	v_cvt_pk_bf16_f32 v100, v100, v101
	v_cvt_pk_bf16_f32 v101, v106, v107
	global_store_dwordx4 v[224:225], v[98:101], off offset:256
	s_nop 1
	v_lshl_add_u64 v[224:225], v[224:225], 0, s[92:93]
	global_load_dwordx4 v[210:213], v[222:223], off offset:256
	v_lshl_add_u64 v[222:223], v[222:223], 0, s[92:93]
	s_waitcnt vmcnt(13)
	v_lshlrev_b32_e32 v98, 16, v214
	v_and_b32_e32 v99, 0xffff0000, v214
	v_lshlrev_b32_e32 v100, 16, v215
	v_and_b32_e32 v101, 0xffff0000, v215
	v_lshlrev_b32_e32 v102, 16, v216
	v_and_b32_e32 v103, 0xffff0000, v216
	v_lshlrev_b32_e32 v104, 16, v217
	v_and_b32_e32 v105, 0xffff0000, v217
	v_pk_fma_f32 v[94:95], v[94:95], v[82:83], v[98:99]
	v_pk_fma_f32 v[98:99], v[92:93], v[88:89], v[104:105]
	v_pk_fma_f32 v[92:93], v[90:91], v[86:87], v[102:103]
	v_pk_fma_f32 v[96:97], v[96:97], v[84:85], v[100:101]
	v_cvt_pk_bf16_f32 v90, v94, v95
	s_nop 0
	v_cvt_pk_bf16_f32 v91, v96, v97
	v_cvt_pk_bf16_f32 v92, v92, v93
	v_cvt_pk_bf16_f32 v93, v98, v99
	global_store_dwordx4 v[224:225], v[90:93], off
	s_nop 1
	global_load_dwordx4 v[214:217], v[222:223], off
	s_waitcnt vmcnt(14)
	v_lshlrev_b32_e32 v90, 16, v218
	v_and_b32_e32 v91, 0xffff0000, v218
	v_lshlrev_b32_e32 v92, 16, v219
	v_and_b32_e32 v93, 0xffff0000, v219
	v_lshlrev_b32_e32 v94, 16, v220
	v_and_b32_e32 v95, 0xffff0000, v220
	v_lshlrev_b32_e32 v96, 16, v221
	v_and_b32_e32 v97, 0xffff0000, v221
	v_pk_fma_f32 v[72:73], v[72:73], v[76:77], v[92:93]
	v_pk_fma_f32 v[70:71], v[70:71], v[74:75], v[90:91]
	v_pk_fma_f32 v[90:91], v[68:69], v[80:81], v[96:97]
	v_pk_fma_f32 v[68:69], v[66:67], v[78:79], v[94:95]
	v_cvt_pk_bf16_f32 v66, v70, v71
	v_cvt_pk_bf16_f32 v67, v72, v73
	v_cvt_pk_bf16_f32 v68, v68, v69
	v_cvt_pk_bf16_f32 v69, v90, v91
	global_store_dwordx4 v[224:225], v[66:69], off offset:256
	s_nop 1
	v_lshl_add_u64 v[224:225], v[224:225], 0, s[94:95]
	global_load_dwordx4 v[218:221], v[222:223], off offset:256
	s_waitcnt vmcnt(14)
	v_lshlrev_b32_e32 v66, 16, v180
	v_and_b32_e32 v67, 0xffff0000, v180
	v_lshlrev_b32_e32 v68, 16, v181
	v_and_b32_e32 v69, 0xffff0000, v181
	v_lshlrev_b32_e32 v70, 16, v182
	v_and_b32_e32 v71, 0xffff0000, v182
	v_lshlrev_b32_e32 v72, 16, v183
	v_and_b32_e32 v73, 0xffff0000, v183
	v_pk_fma_f32 v[62:63], v[62:63], v[82:83], v[66:67]
	v_pk_fma_f32 v[66:67], v[60:61], v[88:89], v[72:73]
	v_pk_fma_f32 v[60:61], v[58:59], v[86:87], v[70:71]
	v_pk_fma_f32 v[64:65], v[64:65], v[84:85], v[68:69]
	v_cvt_pk_bf16_f32 v58, v62, v63
	s_nop 0
	v_cvt_pk_bf16_f32 v59, v64, v65
	v_cvt_pk_bf16_f32 v60, v60, v61
	v_cvt_pk_bf16_f32 v61, v66, v67
	global_store_dwordx4 v[224:225], v[58:61], off
	s_nop 1
	s_waitcnt vmcnt(13)
	v_lshlrev_b32_e32 v58, 16, v184
	v_and_b32_e32 v59, 0xffff0000, v184
	v_lshlrev_b32_e32 v60, 16, v185
	v_and_b32_e32 v61, 0xffff0000, v185
	v_lshlrev_b32_e32 v62, 16, v186
	v_and_b32_e32 v63, 0xffff0000, v186
	v_lshlrev_b32_e32 v64, 16, v187
	v_and_b32_e32 v65, 0xffff0000, v187
	v_pk_fma_f32 v[56:57], v[56:57], v[76:77], v[60:61]
	v_pk_fma_f32 v[54:55], v[54:55], v[74:75], v[58:59]
	v_pk_fma_f32 v[58:59], v[52:53], v[80:81], v[64:65]
	v_pk_fma_f32 v[52:53], v[50:51], v[78:79], v[62:63]
	v_cvt_pk_bf16_f32 v50, v54, v55
	v_cvt_pk_bf16_f32 v51, v56, v57
	v_cvt_pk_bf16_f32 v52, v52, v53
	v_cvt_pk_bf16_f32 v53, v58, v59
	global_store_dwordx4 v[224:225], v[50:53], off offset:256
	s_nop 1
	v_lshl_add_u64 v[224:225], v[224:225], 0, s[92:93]
	s_waitcnt vmcnt(12)
; __device__ __forceinline__ unsigned cvt_pk_bf16(float lo, float hi) { unsigned r; asm volatile("v_cvt_pk_bf16_f32 %0, %1, %2" : "=v"(r) : "v"(lo), "v"(hi)); return r; }
;     __device__ __forceinline__ void operator()(const f32x4 (&acc)[2][2][4][2], const Unit& u, int wr, int wc, int fr, int fq) const {
;     ...
;         for (int ai = 0; ai < 2; ++ai)
; #pragma unroll
;             for (int m = 0; m < 4; ++m) { const size_t ro = (size_t)(row0 + ai * HALF + m * 16) * DM + col0;
; #pragma unroll
;                 for (int bj = 0; bj < 2; ++bj) {
;                     f32x4 h0, h1;
;                     if (xin) { h0 = *(const f32x4*)(xin + ro + bj * HALF); h1 = *(const f32x4*)(xin + ro + bj * HALF + 4); }
;                     else { const u32x4 hb = *(const u32x4*)(hin + ro + bj * HALF);
;                         h0 = (f32x4){__builtin_bit_cast(float, hb.x << 16), __builtin_bit_cast(float, hb.x & 0xffff0000u), __builtin_bit_cast(float, hb.y << 16), __builtin_bit_cast(float, hb.y & 0xffff0000u)};
;                         h1 = (f32x4){__builtin_bit_cast(float, hb.z << 16), __builtin_bit_cast(float, hb.z & 0xffff0000u), __builtin_bit_cast(float, hb.w << 16), __builtin_bit_cast(float, hb.w & 0xffff0000u)}; }
;                     const f32x4 o0 = h0 + gv[bj][0] * acc[ai][bj][m][0], o1 = h1 + gv[bj][1] * acc[ai][bj][m][1];
;                     u32x4 w; w.x = cvt_pk_bf16(o0[0], o0[1]); w.y = cvt_pk_bf16(o0[2], o0[3]); w.z = cvt_pk_bf16(o1[0], o1[1]); w.w = cvt_pk_bf16(o1[2], o1[3]);
;                     *(u32x4*)(hout + ro + bj * HALF) = w; } }
	v_lshlrev_b32_e32 v50, 16, v188
	v_and_b32_e32 v51, 0xffff0000, v188
	v_lshlrev_b32_e32 v52, 16, v189
	v_and_b32_e32 v53, 0xffff0000, v189
	v_lshlrev_b32_e32 v54, 16, v190
	v_and_b32_e32 v55, 0xffff0000, v190
	v_lshlrev_b32_e32 v56, 16, v191
	v_and_b32_e32 v57, 0xffff0000, v191
	v_pk_fma_f32 v[46:47], v[46:47], v[82:83], v[50:51]
	v_pk_fma_f32 v[50:51], v[44:45], v[88:89], v[56:57]
	v_pk_fma_f32 v[44:45], v[42:43], v[86:87], v[54:55]
	v_pk_fma_f32 v[48:49], v[48:49], v[84:85], v[52:53]
	v_cvt_pk_bf16_f32 v42, v46, v47
	s_nop 0
	v_cvt_pk_bf16_f32 v43, v48, v49
	v_cvt_pk_bf16_f32 v44, v44, v45
	v_cvt_pk_bf16_f32 v45, v50, v51
	global_store_dwordx4 v[224:225], v[42:45], off
	s_nop 1
	s_waitcnt vmcnt(11)
	v_lshlrev_b32_e32 v42, 16, v202
	v_and_b32_e32 v43, 0xffff0000, v202
	v_lshlrev_b32_e32 v44, 16, v203
	v_and_b32_e32 v45, 0xffff0000, v203
	v_lshlrev_b32_e32 v46, 16, v204
	v_and_b32_e32 v47, 0xffff0000, v204
	v_lshlrev_b32_e32 v48, 16, v205
	v_and_b32_e32 v49, 0xffff0000, v205
	v_pk_fma_f32 v[40:41], v[40:41], v[76:77], v[44:45]
	v_pk_fma_f32 v[38:39], v[38:39], v[74:75], v[42:43]
	v_pk_fma_f32 v[42:43], v[36:37], v[80:81], v[48:49]
	v_pk_fma_f32 v[36:37], v[34:35], v[78:79], v[46:47]
	v_cvt_pk_bf16_f32 v34, v38, v39
	v_cvt_pk_bf16_f32 v35, v40, v41
	v_cvt_pk_bf16_f32 v36, v36, v37
	v_cvt_pk_bf16_f32 v37, v42, v43
	global_store_dwordx4 v[224:225], v[34:37], off offset:256
	s_nop 1
	v_lshl_add_u64 v[224:225], v[224:225], 0, s[92:93]
	s_waitcnt vmcnt(10)
	v_lshlrev_b32_e32 v34, 16, v206
	v_and_b32_e32 v35, 0xffff0000, v206
	v_lshlrev_b32_e32 v36, 16, v207
	v_and_b32_e32 v37, 0xffff0000, v207
	v_lshlrev_b32_e32 v38, 16, v208
	v_and_b32_e32 v39, 0xffff0000, v208
	v_lshlrev_b32_e32 v40, 16, v209
	v_and_b32_e32 v41, 0xffff0000, v209
	v_pk_fma_f32 v[30:31], v[30:31], v[82:83], v[34:35]
	v_pk_fma_f32 v[34:35], v[28:29], v[88:89], v[40:41]
	v_pk_fma_f32 v[28:29], v[26:27], v[86:87], v[38:39]
	v_pk_fma_f32 v[32:33], v[32:33], v[84:85], v[36:37]
	v_cvt_pk_bf16_f32 v26, v30, v31
	s_nop 0
	v_cvt_pk_bf16_f32 v27, v32, v33
	v_cvt_pk_bf16_f32 v28, v28, v29
	v_cvt_pk_bf16_f32 v29, v34, v35
	global_store_dwordx4 v[224:225], v[26:29], off
	s_nop 1
	s_waitcnt vmcnt(9)
	v_lshlrev_b32_e32 v26, 16, v210
	v_and_b32_e32 v27, 0xffff0000, v210
	v_lshlrev_b32_e32 v28, 16, v211
	v_and_b32_e32 v29, 0xffff0000, v211
	v_lshlrev_b32_e32 v30, 16, v212
	v_and_b32_e32 v31, 0xffff0000, v212
	v_lshlrev_b32_e32 v32, 16, v213
	v_and_b32_e32 v33, 0xffff0000, v213
	v_pk_fma_f32 v[24:25], v[24:25], v[76:77], v[28:29]
	v_pk_fma_f32 v[22:23], v[22:23], v[74:75], v[26:27]
	v_pk_fma_f32 v[26:27], v[20:21], v[80:81], v[32:33]
	v_pk_fma_f32 v[20:21], v[18:19], v[78:79], v[30:31]
	v_cvt_pk_bf16_f32 v18, v22, v23
	v_cvt_pk_bf16_f32 v19, v24, v25
	v_cvt_pk_bf16_f32 v20, v20, v21
	v_cvt_pk_bf16_f32 v21, v26, v27
	global_store_dwordx4 v[224:225], v[18:21], off offset:256
	s_nop 1
	v_lshl_add_u64 v[224:225], v[224:225], 0, s[92:93]
	s_waitcnt vmcnt(8)
	v_lshlrev_b32_e32 v18, 16, v214
	v_and_b32_e32 v19, 0xffff0000, v214
	v_lshlrev_b32_e32 v20, 16, v215
	v_and_b32_e32 v21, 0xffff0000, v215
	v_lshlrev_b32_e32 v22, 16, v216
	v_and_b32_e32 v23, 0xffff0000, v216
	v_lshlrev_b32_e32 v24, 16, v217
	v_and_b32_e32 v25, 0xffff0000, v217
	v_pk_fma_f32 v[14:15], v[14:15], v[82:83], v[18:19]
	v_pk_fma_f32 v[18:19], v[12:13], v[88:89], v[24:25]
	v_pk_fma_f32 v[12:13], v[10:11], v[86:87], v[22:23]
	v_pk_fma_f32 v[16:17], v[16:17], v[84:85], v[20:21]
	v_cvt_pk_bf16_f32 v10, v14, v15
	s_nop 0
	v_cvt_pk_bf16_f32 v11, v16, v17
	v_cvt_pk_bf16_f32 v12, v12, v13
	v_cvt_pk_bf16_f32 v13, v18, v19
	global_store_dwordx4 v[224:225], v[10:13], off
	s_nop 1
	s_waitcnt vmcnt(7)
	v_lshlrev_b32_e32 v10, 16, v218
	v_and_b32_e32 v11, 0xffff0000, v218
	v_lshlrev_b32_e32 v12, 16, v219
	v_and_b32_e32 v13, 0xffff0000, v219
	v_lshlrev_b32_e32 v14, 16, v220
	v_and_b32_e32 v15, 0xffff0000, v220
	v_lshlrev_b32_e32 v16, 16, v221
	v_and_b32_e32 v17, 0xffff0000, v221
	v_pk_fma_f32 v[6:7], v[6:7], v[74:75], v[10:11]
	v_pk_fma_f32 v[10:11], v[4:5], v[80:81], v[16:17]
	v_pk_fma_f32 v[4:5], v[2:3], v[78:79], v[14:15]
	v_pk_fma_f32 v[8:9], v[8:9], v[76:77], v[12:13]
	v_cvt_pk_bf16_f32 v2, v6, v7
	s_nop 0
	v_cvt_pk_bf16_f32 v3, v8, v9
	v_cvt_pk_bf16_f32 v4, v4, v5
	v_cvt_pk_bf16_f32 v5, v10, v11
	global_store_dwordx4 v[224:225], v[2:5], off offset:256
	s_nop 1
	s_and_b64 vcc, exec, s[40:41]
	s_mov_b64 s[28:29], -1
	s_branch .Lepi_done
